# speedup vs baseline: 1.0054x; 1.0046x over previous
.LBB3_31:
	v_add_u32_e32 v31, s2, v11
	v_add_u32_e32 v13, s2, v12
	ds_read_b128 v[14:17], v31
	s_waitcnt vmcnt(0)
	ds_read_b128 v[18:21], v31 offset:16
	ds_read_b128 v[22:25], v31 offset:256
	ds_read_b128 v[26:29], v31 offset:272
	ds_read_b128 v[32:35], v31 offset:512
	ds_read_b128 v[36:39], v31 offset:528
	ds_read_b128 v[40:43], v31 offset:768
	ds_read_b128 v[44:47], v31 offset:784
	ds_read_b128 v[48:51], v31 offset:1024
	ds_read_b128 v[52:55], v31 offset:1040
	ds_read_b128 v[56:59], v31 offset:1280
	ds_read_b128 v[60:63], v31 offset:1296
	ds_read2st64_b32 v[96:97], v13 offset1:1
	ds_read2st64_b32 v[98:99], v13 offset0:2 offset1:3
	ds_read2st64_b32 v[100:101], v13 offset0:4 offset1:5
	ds_read2st64_b32 v[102:103], v13 offset0:6 offset1:7
	ds_read_b128 v[64:67], v31 offset:1536
	ds_read_b128 v[68:71], v31 offset:1552
	ds_read_b128 v[72:75], v31 offset:1792
	ds_read_b128 v[76:79], v31 offset:1808
	ds_read2st64_b32 v[104:105], v13 offset0:8 offset1:9
	ds_read_b128 v[80:83], v31 offset:2048
	ds_read_b128 v[84:87], v31 offset:2064
	ds_read_b128 v[88:91], v31 offset:2304
	ds_read_b128 v[92:95], v31 offset:2320
	s_waitcnt lgkmcnt(12)
	v_fmac_f32_e32 v6, v96, v14
	v_fmac_f32_e32 v7, v96, v15
	v_fmac_f32_e32 v8, v96, v16
	v_fmac_f32_e32 v9, v96, v17
	v_fmac_f32_e32 v2, v96, v18
	v_fmac_f32_e32 v3, v96, v19
	v_fmac_f32_e32 v4, v96, v20
	v_fmac_f32_e32 v5, v96, v21
	v_fmac_f32_e32 v6, v97, v22
	v_fmac_f32_e32 v7, v97, v23
	v_fmac_f32_e32 v8, v97, v24
	v_fmac_f32_e32 v9, v97, v25
	v_fmac_f32_e32 v2, v97, v26
	v_fmac_f32_e32 v3, v97, v27
	v_fmac_f32_e32 v4, v97, v28
	v_fmac_f32_e32 v5, v97, v29
	s_waitcnt lgkmcnt(11)
	v_fmac_f32_e32 v6, v98, v32
	v_fmac_f32_e32 v7, v98, v33
	v_fmac_f32_e32 v8, v98, v34
	v_fmac_f32_e32 v9, v98, v35
	v_fmac_f32_e32 v2, v98, v36
	v_fmac_f32_e32 v3, v98, v37
	v_fmac_f32_e32 v4, v98, v38
	v_fmac_f32_e32 v5, v98, v39
	v_fmac_f32_e32 v6, v99, v40
	v_fmac_f32_e32 v7, v99, v41
	v_fmac_f32_e32 v8, v99, v42
	v_fmac_f32_e32 v9, v99, v43
	v_fmac_f32_e32 v2, v99, v44
	v_fmac_f32_e32 v3, v99, v45
	v_fmac_f32_e32 v4, v99, v46
	v_fmac_f32_e32 v5, v99, v47
	s_waitcnt lgkmcnt(10)
	v_fmac_f32_e32 v6, v100, v48
	v_fmac_f32_e32 v7, v100, v49
	v_fmac_f32_e32 v8, v100, v50
	v_fmac_f32_e32 v9, v100, v51
	v_fmac_f32_e32 v2, v100, v52
	v_fmac_f32_e32 v3, v100, v53
	v_fmac_f32_e32 v4, v100, v54
	v_fmac_f32_e32 v5, v100, v55
	v_fmac_f32_e32 v6, v101, v56
	v_fmac_f32_e32 v7, v101, v57
	v_fmac_f32_e32 v8, v101, v58
	v_fmac_f32_e32 v9, v101, v59
	v_fmac_f32_e32 v2, v101, v60
	v_fmac_f32_e32 v3, v101, v61
	v_fmac_f32_e32 v4, v101, v62
	v_fmac_f32_e32 v5, v101, v63
	s_waitcnt lgkmcnt(7)
	v_fmac_f32_e32 v6, v102, v64
	v_fmac_f32_e32 v7, v102, v65
	v_fmac_f32_e32 v8, v102, v66
	v_fmac_f32_e32 v9, v102, v67
	v_fmac_f32_e32 v2, v102, v68
	v_fmac_f32_e32 v3, v102, v69
	v_fmac_f32_e32 v4, v102, v70
	v_fmac_f32_e32 v5, v102, v71
	s_waitcnt lgkmcnt(5)
	v_fmac_f32_e32 v6, v103, v72
	v_fmac_f32_e32 v7, v103, v73
	v_fmac_f32_e32 v8, v103, v74
	v_fmac_f32_e32 v9, v103, v75
	v_fmac_f32_e32 v2, v103, v76
	v_fmac_f32_e32 v3, v103, v77
	v_fmac_f32_e32 v4, v103, v78
	v_fmac_f32_e32 v5, v103, v79
	s_addk_i32 s2, 0xa00
	s_waitcnt lgkmcnt(2)
	v_fmac_f32_e32 v6, v104, v80
	v_fmac_f32_e32 v7, v104, v81
	v_fmac_f32_e32 v8, v104, v82
	v_fmac_f32_e32 v9, v104, v83
	v_fmac_f32_e32 v2, v104, v84
	v_fmac_f32_e32 v3, v104, v85
	v_fmac_f32_e32 v4, v104, v86
	v_fmac_f32_e32 v5, v104, v87
	s_cmpk_eq_i32 s2, 0x6400
	s_waitcnt lgkmcnt(0)
	v_fmac_f32_e32 v6, v105, v88
	v_fmac_f32_e32 v7, v105, v89
	v_fmac_f32_e32 v8, v105, v90
	v_fmac_f32_e32 v9, v105, v91
	v_fmac_f32_e32 v2, v105, v92
	v_fmac_f32_e32 v3, v105, v93
	v_fmac_f32_e32 v4, v105, v94
	v_fmac_f32_e32 v5, v105, v95
	s_cbranch_scc0 .LBB3_31
	s_and_saveexec_b64 s[2:3], vcc
	s_cbranch_execz .LBB3_34
	v_add_u32_e32 v12, 0xfa0, v30
	v_mov_b32_e32 v13, 0
	v_lshlrev_b64 v[14:15], 8, v[12:13]
	v_lshl_add_u64 v[14:15], s[16:17], 0, v[14:15]
	v_lshlrev_b32_e32 v12, 2, v10
	v_lshl_add_u64 v[10:11], v[14:15], 0, v[12:13]
	global_store_dwordx4 v[10:11], v[6:9], off
	global_store_dwordx4 v[10:11], v[2:5], off offset:16
